# gate epilogue rewritten: fmamk with premultiplied bias, vertical staging, no max/no nops, 3-op pack
# speedup vs baseline: 1.2600x; 1.0094x over previous
.LBB0_796:
	global_load_dwordx4 v[8:11], v[6:7], off
	v_add_u32_e32 v2, 0x200, v2
	v_cmp_lt_i32_e32 vcc, s77, v2
	v_lshl_add_u64 v[6:7], v[6:7], 0, s[72:73]
	s_or_b64 s[8:9], vcc, s[8:9]
	s_waitcnt vmcnt(0)
	v_mul_f32_e32 v8, 0xbfb8aa3b, v8
	v_mul_f32_e32 v9, 0xbfb8aa3b, v9
	v_mul_f32_e32 v10, 0xbfb8aa3b, v10
	v_mul_f32_e32 v11, 0xbfb8aa3b, v11
	ds_write_b128 v4, v[8:11]
	v_add_u32_e32 v4, 0x2000, v4
	s_andn2_b64 exec, exec, s[8:9]
	s_cbranch_execnz .LBB0_796

.LBB0_853:
	s_waitcnt lgkmcnt(0)
	v_fmamk_f32 v160, v160, 0xbfb8aa3b, v184
	v_fmamk_f32 v161, v161, 0xbfb8aa3b, v185
	v_fmamk_f32 v162, v162, 0xbfb8aa3b, v186
	v_fmamk_f32 v163, v163, 0xbfb8aa3b, v187
	v_fmamk_f32 v156, v156, 0xbfb8aa3b, v180
	v_fmamk_f32 v157, v157, 0xbfb8aa3b, v181
	v_fmamk_f32 v158, v158, 0xbfb8aa3b, v182
	v_fmamk_f32 v159, v159, 0xbfb8aa3b, v183
	v_fmamk_f32 v152, v152, 0xbfb8aa3b, v188
	v_fmamk_f32 v153, v153, 0xbfb8aa3b, v189
	v_fmamk_f32 v154, v154, 0xbfb8aa3b, v190
	v_fmamk_f32 v155, v155, 0xbfb8aa3b, v191
	v_fmamk_f32 v148, v148, 0xbfb8aa3b, v192
	v_fmamk_f32 v149, v149, 0xbfb8aa3b, v193
	v_fmamk_f32 v150, v150, 0xbfb8aa3b, v194
	v_fmamk_f32 v151, v151, 0xbfb8aa3b, v195
	v_mov_b32_e32 v223, 0
	s_add_i32 s19, s87, -11
	s_lshr_b32 s20, s19, 2
	v_mov_b32_e32 v184, s20
	v_mov_b32_e32 v185, v3
	v_mad_i64_i32 v[184:185], s[20:21], v220, 3, v[184:185]
	v_lshlrev_b64 v[184:185], 10, v[184:185]
	s_lshl_b32 s19, s19, 8
	s_and_b32 s34, s19, 0x300
	v_lshl_add_u64 v[184:185], s[46:47], 0, v[184:185]
	v_lshl_add_u64 v[184:185], v[184:185], 0, s[34:35]
	v_lshl_add_u64 v[186:187], v[184:185], 0, v[2:3]
	v_exp_f32_e32 v160, v160
	v_exp_f32_e32 v161, v161
	v_exp_f32_e32 v162, v162
	v_exp_f32_e32 v163, v163
	v_exp_f32_e32 v156, v156
	v_exp_f32_e32 v157, v157
	v_exp_f32_e32 v158, v158
	v_exp_f32_e32 v159, v159
	v_exp_f32_e32 v152, v152
	v_exp_f32_e32 v153, v153
	v_exp_f32_e32 v154, v154
	v_exp_f32_e32 v155, v155
	v_exp_f32_e32 v148, v148
	v_exp_f32_e32 v149, v149
	v_exp_f32_e32 v150, v150
	v_exp_f32_e32 v151, v151
	v_add_f32_e32 v160, 1.0, v160
	v_add_f32_e32 v161, 1.0, v161
	v_add_f32_e32 v162, 1.0, v162
	v_add_f32_e32 v163, 1.0, v163
	v_add_f32_e32 v156, 1.0, v156
	v_add_f32_e32 v157, 1.0, v157
	v_add_f32_e32 v158, 1.0, v158
	v_add_f32_e32 v159, 1.0, v159
	v_add_f32_e32 v152, 1.0, v152
	v_add_f32_e32 v153, 1.0, v153
	v_add_f32_e32 v154, 1.0, v154
	v_add_f32_e32 v155, 1.0, v155
	v_add_f32_e32 v148, 1.0, v148
	v_add_f32_e32 v149, 1.0, v149
	v_add_f32_e32 v150, 1.0, v150
	v_add_f32_e32 v151, 1.0, v151
	v_rcp_f32_e32 v160, v160
	v_rcp_f32_e32 v161, v161
	v_rcp_f32_e32 v162, v162
	v_rcp_f32_e32 v163, v163
	v_rcp_f32_e32 v156, v156
	v_rcp_f32_e32 v157, v157
	v_rcp_f32_e32 v158, v158
	v_rcp_f32_e32 v159, v159
	v_rcp_f32_e32 v152, v152
	v_rcp_f32_e32 v153, v153
	v_rcp_f32_e32 v154, v154
	v_rcp_f32_e32 v155, v155
	v_rcp_f32_e32 v148, v148
	v_rcp_f32_e32 v149, v149
	v_rcp_f32_e32 v150, v150
	v_rcp_f32_e32 v151, v151
	v_add_u32_e32 v160, 0xc4820000, v160
	v_add_u32_e32 v161, 0xc4820000, v161
	v_add_u32_e32 v162, 0xc4820000, v162
	v_add_u32_e32 v163, 0xc4820000, v163
	v_add_u32_e32 v156, 0xc4820000, v156
	v_add_u32_e32 v157, 0xc4820000, v157
	v_add_u32_e32 v158, 0xc4820000, v158
	v_add_u32_e32 v159, 0xc4820000, v159
	v_add_u32_e32 v152, 0xc4820000, v152
	v_add_u32_e32 v153, 0xc4820000, v153
	v_add_u32_e32 v154, 0xc4820000, v154
	v_add_u32_e32 v155, 0xc4820000, v155
	v_add_u32_e32 v148, 0xc4820000, v148
	v_add_u32_e32 v149, 0xc4820000, v149
	v_add_u32_e32 v150, 0xc4820000, v150
	v_add_u32_e32 v151, 0xc4820000, v151
	v_ashrrev_i32_e32 v160, 18, v160
	v_ashrrev_i32_e32 v161, 18, v161
	v_ashrrev_i32_e32 v162, 18, v162
	v_ashrrev_i32_e32 v163, 18, v163
	v_ashrrev_i32_e32 v156, 18, v156
	v_ashrrev_i32_e32 v157, 18, v157
	v_ashrrev_i32_e32 v158, 18, v158
	v_ashrrev_i32_e32 v159, 18, v159
	v_ashrrev_i32_e32 v152, 18, v152
	v_ashrrev_i32_e32 v153, 18, v153
	v_ashrrev_i32_e32 v154, 18, v154
	v_ashrrev_i32_e32 v155, 18, v155
	v_ashrrev_i32_e32 v148, 18, v148
	v_ashrrev_i32_e32 v149, 18, v149
	v_ashrrev_i32_e32 v150, 18, v150
	v_ashrrev_i32_e32 v151, 18, v151
	v_med3_i32 v160, v160, 0, v236
	v_med3_i32 v161, v161, 0, v236
	v_med3_i32 v162, v162, 0, v236
	v_med3_i32 v163, v163, 0, v236
	v_med3_i32 v156, v156, 0, v236
	v_med3_i32 v157, v157, 0, v236
	v_med3_i32 v158, v158, 0, v236
	v_med3_i32 v159, v159, 0, v236
	v_med3_i32 v152, v152, 0, v236
	v_med3_i32 v153, v153, 0, v236
	v_med3_i32 v154, v154, 0, v236
	v_med3_i32 v155, v155, 0, v236
	v_med3_i32 v148, v148, 0, v236
	v_med3_i32 v149, v149, 0, v236
	v_med3_i32 v150, v150, 0, v236
	v_med3_i32 v151, v151, 0, v236
	v_lshl_or_b32 v160, v161, 8, v160
	v_lshl_or_b32 v162, v163, 8, v162
	v_lshl_or_b32 v180, v162, 16, v160
	v_lshl_or_b32 v156, v157, 8, v156
	v_lshl_or_b32 v158, v159, 8, v158
	v_lshl_or_b32 v181, v158, 16, v156
	v_lshl_or_b32 v152, v153, 8, v152
	v_lshl_or_b32 v154, v155, 8, v154
	v_lshl_or_b32 v182, v154, 16, v152
	v_lshl_or_b32 v148, v149, 8, v148
	v_lshl_or_b32 v150, v151, 8, v150
	v_lshl_or_b32 v183, v150, 16, v148
	global_store_dwordx4 v[186:187], v[180:183], off
	s_and_b64 vcc, exec, s[40:41]
	s_mov_b64 s[26:27], -1
	s_cbranch_vccz .LBB0_925

.LBB0_855:
	s_waitcnt lgkmcnt(0)
	v_fmamk_f32 v128, v128, 0xbfb8aa3b, v168
	v_fmamk_f32 v129, v129, 0xbfb8aa3b, v169
	v_fmamk_f32 v130, v130, 0xbfb8aa3b, v170
	v_fmamk_f32 v131, v131, 0xbfb8aa3b, v171
	v_fmamk_f32 v124, v124, 0xbfb8aa3b, v164
	v_fmamk_f32 v125, v125, 0xbfb8aa3b, v165
	v_fmamk_f32 v126, v126, 0xbfb8aa3b, v166
	v_fmamk_f32 v127, v127, 0xbfb8aa3b, v167
	v_fmamk_f32 v120, v120, 0xbfb8aa3b, v172
	v_fmamk_f32 v121, v121, 0xbfb8aa3b, v173
	v_fmamk_f32 v122, v122, 0xbfb8aa3b, v174
	v_fmamk_f32 v123, v123, 0xbfb8aa3b, v175
	v_fmamk_f32 v116, v116, 0xbfb8aa3b, v176
	v_fmamk_f32 v117, v117, 0xbfb8aa3b, v177
	v_fmamk_f32 v118, v118, 0xbfb8aa3b, v178
	v_fmamk_f32 v119, v119, 0xbfb8aa3b, v179
	v_mov_b32_e32 v150, v223
	s_add_i32 s19, s87, -11
	s_lshr_b32 s20, s19, 2
	v_mov_b32_e32 v168, s20
	v_mov_b32_e32 v169, v3
	v_mad_i64_i32 v[168:169], s[20:21], v226, 3, v[168:169]
	v_lshlrev_b64 v[168:169], 10, v[168:169]
	s_lshl_b32 s19, s19, 8
	s_and_b32 s34, s19, 0x300
	v_lshl_add_u64 v[168:169], s[46:47], 0, v[168:169]
	v_lshl_add_u64 v[168:169], v[168:169], 0, s[34:35]
	v_lshl_add_u64 v[170:171], v[168:169], 0, v[2:3]
	v_exp_f32_e32 v128, v128
	v_exp_f32_e32 v129, v129
	v_exp_f32_e32 v130, v130
	v_exp_f32_e32 v131, v131
	v_exp_f32_e32 v124, v124
	v_exp_f32_e32 v125, v125
	v_exp_f32_e32 v126, v126
	v_exp_f32_e32 v127, v127
	v_exp_f32_e32 v120, v120
	v_exp_f32_e32 v121, v121
	v_exp_f32_e32 v122, v122
	v_exp_f32_e32 v123, v123
	v_exp_f32_e32 v116, v116
	v_exp_f32_e32 v117, v117
	v_exp_f32_e32 v118, v118
	v_exp_f32_e32 v119, v119
	v_add_f32_e32 v128, 1.0, v128
	v_add_f32_e32 v129, 1.0, v129
	v_add_f32_e32 v130, 1.0, v130
	v_add_f32_e32 v131, 1.0, v131
	v_add_f32_e32 v124, 1.0, v124
	v_add_f32_e32 v125, 1.0, v125
	v_add_f32_e32 v126, 1.0, v126
	v_add_f32_e32 v127, 1.0, v127
	v_add_f32_e32 v120, 1.0, v120
	v_add_f32_e32 v121, 1.0, v121
	v_add_f32_e32 v122, 1.0, v122
	v_add_f32_e32 v123, 1.0, v123
	v_add_f32_e32 v116, 1.0, v116
	v_add_f32_e32 v117, 1.0, v117
	v_add_f32_e32 v118, 1.0, v118
	v_add_f32_e32 v119, 1.0, v119
	v_rcp_f32_e32 v128, v128
	v_rcp_f32_e32 v129, v129
	v_rcp_f32_e32 v130, v130
	v_rcp_f32_e32 v131, v131
	v_rcp_f32_e32 v124, v124
	v_rcp_f32_e32 v125, v125
	v_rcp_f32_e32 v126, v126
	v_rcp_f32_e32 v127, v127
	v_rcp_f32_e32 v120, v120
	v_rcp_f32_e32 v121, v121
	v_rcp_f32_e32 v122, v122
	v_rcp_f32_e32 v123, v123
	v_rcp_f32_e32 v116, v116
	v_rcp_f32_e32 v117, v117
	v_rcp_f32_e32 v118, v118
	v_rcp_f32_e32 v119, v119
	v_add_u32_e32 v128, 0xc4820000, v128
	v_add_u32_e32 v129, 0xc4820000, v129
	v_add_u32_e32 v130, 0xc4820000, v130
	v_add_u32_e32 v131, 0xc4820000, v131
	v_add_u32_e32 v124, 0xc4820000, v124
	v_add_u32_e32 v125, 0xc4820000, v125
	v_add_u32_e32 v126, 0xc4820000, v126
	v_add_u32_e32 v127, 0xc4820000, v127
	v_add_u32_e32 v120, 0xc4820000, v120
	v_add_u32_e32 v121, 0xc4820000, v121
	v_add_u32_e32 v122, 0xc4820000, v122
	v_add_u32_e32 v123, 0xc4820000, v123
	v_add_u32_e32 v116, 0xc4820000, v116
	v_add_u32_e32 v117, 0xc4820000, v117
	v_add_u32_e32 v118, 0xc4820000, v118
	v_add_u32_e32 v119, 0xc4820000, v119
	v_ashrrev_i32_e32 v128, 18, v128
	v_ashrrev_i32_e32 v129, 18, v129
	v_ashrrev_i32_e32 v130, 18, v130
	v_ashrrev_i32_e32 v131, 18, v131
	v_ashrrev_i32_e32 v124, 18, v124
	v_ashrrev_i32_e32 v125, 18, v125
	v_ashrrev_i32_e32 v126, 18, v126
	v_ashrrev_i32_e32 v127, 18, v127
	v_ashrrev_i32_e32 v120, 18, v120
	v_ashrrev_i32_e32 v121, 18, v121
	v_ashrrev_i32_e32 v122, 18, v122
	v_ashrrev_i32_e32 v123, 18, v123
	v_ashrrev_i32_e32 v116, 18, v116
	v_ashrrev_i32_e32 v117, 18, v117
	v_ashrrev_i32_e32 v118, 18, v118
	v_ashrrev_i32_e32 v119, 18, v119
	v_med3_i32 v128, v128, 0, v236
	v_med3_i32 v129, v129, 0, v236
	v_med3_i32 v130, v130, 0, v236
	v_med3_i32 v131, v131, 0, v236
	v_med3_i32 v124, v124, 0, v236
	v_med3_i32 v125, v125, 0, v236
	v_med3_i32 v126, v126, 0, v236
	v_med3_i32 v127, v127, 0, v236
	v_med3_i32 v120, v120, 0, v236
	v_med3_i32 v121, v121, 0, v236
	v_med3_i32 v122, v122, 0, v236
	v_med3_i32 v123, v123, 0, v236
	v_med3_i32 v116, v116, 0, v236
	v_med3_i32 v117, v117, 0, v236
	v_med3_i32 v118, v118, 0, v236
	v_med3_i32 v119, v119, 0, v236
	v_lshl_or_b32 v128, v129, 8, v128
	v_lshl_or_b32 v130, v131, 8, v130
	v_lshl_or_b32 v164, v130, 16, v128
	v_lshl_or_b32 v124, v125, 8, v124
	v_lshl_or_b32 v126, v127, 8, v126
	v_lshl_or_b32 v165, v126, 16, v124
	v_lshl_or_b32 v120, v121, 8, v120
	v_lshl_or_b32 v122, v123, 8, v122
	v_lshl_or_b32 v166, v122, 16, v120
	v_lshl_or_b32 v116, v117, 8, v116
	v_lshl_or_b32 v118, v119, 8, v118
	v_lshl_or_b32 v167, v118, 16, v116
	global_store_dwordx4 v[170:171], v[164:167], off
	s_and_b64 vcc, exec, s[40:41]
	s_mov_b64 s[26:27], -1
	s_cbranch_vccz .LBB0_975

.LBB0_857:
	s_waitcnt lgkmcnt(0)
	v_fmamk_f32 v96, v96, 0xbfb8aa3b, v136
	v_fmamk_f32 v97, v97, 0xbfb8aa3b, v137
	v_fmamk_f32 v98, v98, 0xbfb8aa3b, v138
	v_fmamk_f32 v99, v99, 0xbfb8aa3b, v139
	v_fmamk_f32 v92, v92, 0xbfb8aa3b, v132
	v_fmamk_f32 v93, v93, 0xbfb8aa3b, v133
	v_fmamk_f32 v94, v94, 0xbfb8aa3b, v134
	v_fmamk_f32 v95, v95, 0xbfb8aa3b, v135
	v_fmamk_f32 v88, v88, 0xbfb8aa3b, v140
	v_fmamk_f32 v89, v89, 0xbfb8aa3b, v141
	v_fmamk_f32 v90, v90, 0xbfb8aa3b, v142
	v_fmamk_f32 v91, v91, 0xbfb8aa3b, v143
	v_fmamk_f32 v84, v84, 0xbfb8aa3b, v144
	v_fmamk_f32 v85, v85, 0xbfb8aa3b, v145
	v_fmamk_f32 v86, v86, 0xbfb8aa3b, v146
	v_fmamk_f32 v87, v87, 0xbfb8aa3b, v147
	v_mov_b32_e32 v118, v150
	s_add_i32 s19, s87, -11
	s_lshr_b32 s20, s19, 2
	v_mov_b32_e32 v136, s20
	v_mov_b32_e32 v137, v3
	v_mad_i64_i32 v[136:137], s[20:21], v224, 3, v[136:137]
	v_lshlrev_b64 v[136:137], 10, v[136:137]
	s_lshl_b32 s19, s19, 8
	s_and_b32 s34, s19, 0x300
	v_lshl_add_u64 v[136:137], s[46:47], 0, v[136:137]
	v_lshl_add_u64 v[136:137], v[136:137], 0, s[34:35]
	v_lshl_add_u64 v[138:139], v[136:137], 0, v[2:3]
	v_exp_f32_e32 v96, v96
	v_exp_f32_e32 v97, v97
	v_exp_f32_e32 v98, v98
	v_exp_f32_e32 v99, v99
	v_exp_f32_e32 v92, v92
	v_exp_f32_e32 v93, v93
	v_exp_f32_e32 v94, v94
	v_exp_f32_e32 v95, v95
	v_exp_f32_e32 v88, v88
	v_exp_f32_e32 v89, v89
	v_exp_f32_e32 v90, v90
	v_exp_f32_e32 v91, v91
	v_exp_f32_e32 v84, v84
	v_exp_f32_e32 v85, v85
	v_exp_f32_e32 v86, v86
	v_exp_f32_e32 v87, v87
	v_add_f32_e32 v96, 1.0, v96
	v_add_f32_e32 v97, 1.0, v97
	v_add_f32_e32 v98, 1.0, v98
	v_add_f32_e32 v99, 1.0, v99
	v_add_f32_e32 v92, 1.0, v92
	v_add_f32_e32 v93, 1.0, v93
	v_add_f32_e32 v94, 1.0, v94
	v_add_f32_e32 v95, 1.0, v95
	v_add_f32_e32 v88, 1.0, v88
	v_add_f32_e32 v89, 1.0, v89
	v_add_f32_e32 v90, 1.0, v90
	v_add_f32_e32 v91, 1.0, v91
	v_add_f32_e32 v84, 1.0, v84
	v_add_f32_e32 v85, 1.0, v85
	v_add_f32_e32 v86, 1.0, v86
	v_add_f32_e32 v87, 1.0, v87
	v_rcp_f32_e32 v96, v96
	v_rcp_f32_e32 v97, v97
	v_rcp_f32_e32 v98, v98
	v_rcp_f32_e32 v99, v99
	v_rcp_f32_e32 v92, v92
	v_rcp_f32_e32 v93, v93
	v_rcp_f32_e32 v94, v94
	v_rcp_f32_e32 v95, v95
	v_rcp_f32_e32 v88, v88
	v_rcp_f32_e32 v89, v89
	v_rcp_f32_e32 v90, v90
	v_rcp_f32_e32 v91, v91
	v_rcp_f32_e32 v84, v84
	v_rcp_f32_e32 v85, v85
	v_rcp_f32_e32 v86, v86
	v_rcp_f32_e32 v87, v87
	v_add_u32_e32 v96, 0xc4820000, v96
	v_add_u32_e32 v97, 0xc4820000, v97
	v_add_u32_e32 v98, 0xc4820000, v98
	v_add_u32_e32 v99, 0xc4820000, v99
	v_add_u32_e32 v92, 0xc4820000, v92
	v_add_u32_e32 v93, 0xc4820000, v93
	v_add_u32_e32 v94, 0xc4820000, v94
	v_add_u32_e32 v95, 0xc4820000, v95
	v_add_u32_e32 v88, 0xc4820000, v88
	v_add_u32_e32 v89, 0xc4820000, v89
	v_add_u32_e32 v90, 0xc4820000, v90
	v_add_u32_e32 v91, 0xc4820000, v91
	v_add_u32_e32 v84, 0xc4820000, v84
	v_add_u32_e32 v85, 0xc4820000, v85
	v_add_u32_e32 v86, 0xc4820000, v86
	v_add_u32_e32 v87, 0xc4820000, v87
	v_ashrrev_i32_e32 v96, 18, v96
	v_ashrrev_i32_e32 v97, 18, v97
	v_ashrrev_i32_e32 v98, 18, v98
	v_ashrrev_i32_e32 v99, 18, v99
	v_ashrrev_i32_e32 v92, 18, v92
	v_ashrrev_i32_e32 v93, 18, v93
	v_ashrrev_i32_e32 v94, 18, v94
	v_ashrrev_i32_e32 v95, 18, v95
	v_ashrrev_i32_e32 v88, 18, v88
	v_ashrrev_i32_e32 v89, 18, v89
	v_ashrrev_i32_e32 v90, 18, v90
	v_ashrrev_i32_e32 v91, 18, v91
	v_ashrrev_i32_e32 v84, 18, v84
	v_ashrrev_i32_e32 v85, 18, v85
	v_ashrrev_i32_e32 v86, 18, v86
	v_ashrrev_i32_e32 v87, 18, v87
	v_med3_i32 v96, v96, 0, v236
	v_med3_i32 v97, v97, 0, v236
	v_med3_i32 v98, v98, 0, v236
	v_med3_i32 v99, v99, 0, v236
	v_med3_i32 v92, v92, 0, v236
	v_med3_i32 v93, v93, 0, v236
	v_med3_i32 v94, v94, 0, v236
	v_med3_i32 v95, v95, 0, v236
	v_med3_i32 v88, v88, 0, v236
	v_med3_i32 v89, v89, 0, v236
	v_med3_i32 v90, v90, 0, v236
	v_med3_i32 v91, v91, 0, v236
	v_med3_i32 v84, v84, 0, v236
	v_med3_i32 v85, v85, 0, v236
	v_med3_i32 v86, v86, 0, v236
	v_med3_i32 v87, v87, 0, v236
	v_lshl_or_b32 v96, v97, 8, v96
	v_lshl_or_b32 v98, v99, 8, v98
	v_lshl_or_b32 v132, v98, 16, v96
	v_lshl_or_b32 v92, v93, 8, v92
	v_lshl_or_b32 v94, v95, 8, v94
	v_lshl_or_b32 v133, v94, 16, v92
	v_lshl_or_b32 v88, v89, 8, v88
	v_lshl_or_b32 v90, v91, 8, v90
	v_lshl_or_b32 v134, v90, 16, v88
	v_lshl_or_b32 v84, v85, 8, v84
	v_lshl_or_b32 v86, v87, 8, v86
	v_lshl_or_b32 v135, v86, 16, v84
	global_store_dwordx4 v[138:139], v[132:135], off
	s_and_b64 vcc, exec, s[40:41]
	s_mov_b64 s[26:27], -1
	s_cbranch_vccz .LBB0_1025

.LBB0_859:
	s_waitcnt lgkmcnt(0)
	v_fmamk_f32 v80, v80, 0xbfb8aa3b, v104
	v_fmamk_f32 v81, v81, 0xbfb8aa3b, v105
	v_fmamk_f32 v82, v82, 0xbfb8aa3b, v106
	v_fmamk_f32 v83, v83, 0xbfb8aa3b, v107
	v_fmamk_f32 v76, v76, 0xbfb8aa3b, v100
	v_fmamk_f32 v77, v77, 0xbfb8aa3b, v101
	v_fmamk_f32 v78, v78, 0xbfb8aa3b, v102
	v_fmamk_f32 v79, v79, 0xbfb8aa3b, v103
	v_fmamk_f32 v72, v72, 0xbfb8aa3b, v108
	v_fmamk_f32 v73, v73, 0xbfb8aa3b, v109
	v_fmamk_f32 v74, v74, 0xbfb8aa3b, v110
	v_fmamk_f32 v75, v75, 0xbfb8aa3b, v111
	v_fmamk_f32 v68, v68, 0xbfb8aa3b, v112
	v_fmamk_f32 v69, v69, 0xbfb8aa3b, v113
	v_fmamk_f32 v70, v70, 0xbfb8aa3b, v114
	v_fmamk_f32 v71, v71, 0xbfb8aa3b, v115
	v_mov_b32_e32 v142, v118
	s_add_i32 s19, s87, -11
	s_lshr_b32 s20, s19, 2
	v_mov_b32_e32 v104, s20
	v_mov_b32_e32 v105, v3
	v_mad_i64_i32 v[104:105], s[20:21], v222, 3, v[104:105]
	v_lshlrev_b64 v[104:105], 10, v[104:105]
	s_lshl_b32 s19, s19, 8
	s_and_b32 s34, s19, 0x300
	v_lshl_add_u64 v[104:105], s[46:47], 0, v[104:105]
	v_lshl_add_u64 v[104:105], v[104:105], 0, s[34:35]
	v_lshl_add_u64 v[106:107], v[104:105], 0, v[2:3]
	v_exp_f32_e32 v80, v80
	v_exp_f32_e32 v81, v81
	v_exp_f32_e32 v82, v82
	v_exp_f32_e32 v83, v83
	v_exp_f32_e32 v76, v76
	v_exp_f32_e32 v77, v77
	v_exp_f32_e32 v78, v78
	v_exp_f32_e32 v79, v79
	v_exp_f32_e32 v72, v72
	v_exp_f32_e32 v73, v73
	v_exp_f32_e32 v74, v74
	v_exp_f32_e32 v75, v75
	v_exp_f32_e32 v68, v68
	v_exp_f32_e32 v69, v69
	v_exp_f32_e32 v70, v70
	v_exp_f32_e32 v71, v71
	v_add_f32_e32 v80, 1.0, v80
	v_add_f32_e32 v81, 1.0, v81
	v_add_f32_e32 v82, 1.0, v82
	v_add_f32_e32 v83, 1.0, v83
	v_add_f32_e32 v76, 1.0, v76
	v_add_f32_e32 v77, 1.0, v77
	v_add_f32_e32 v78, 1.0, v78
	v_add_f32_e32 v79, 1.0, v79
	v_add_f32_e32 v72, 1.0, v72
	v_add_f32_e32 v73, 1.0, v73
	v_add_f32_e32 v74, 1.0, v74
	v_add_f32_e32 v75, 1.0, v75
	v_add_f32_e32 v68, 1.0, v68
	v_add_f32_e32 v69, 1.0, v69
	v_add_f32_e32 v70, 1.0, v70
	v_add_f32_e32 v71, 1.0, v71
	v_rcp_f32_e32 v80, v80
	v_rcp_f32_e32 v81, v81
	v_rcp_f32_e32 v82, v82
	v_rcp_f32_e32 v83, v83
	v_rcp_f32_e32 v76, v76
	v_rcp_f32_e32 v77, v77
	v_rcp_f32_e32 v78, v78
	v_rcp_f32_e32 v79, v79
	v_rcp_f32_e32 v72, v72
	v_rcp_f32_e32 v73, v73
	v_rcp_f32_e32 v74, v74
	v_rcp_f32_e32 v75, v75
	v_rcp_f32_e32 v68, v68
	v_rcp_f32_e32 v69, v69
	v_rcp_f32_e32 v70, v70
	v_rcp_f32_e32 v71, v71
	v_add_u32_e32 v80, 0xc4820000, v80
	v_add_u32_e32 v81, 0xc4820000, v81
	v_add_u32_e32 v82, 0xc4820000, v82
	v_add_u32_e32 v83, 0xc4820000, v83
	v_add_u32_e32 v76, 0xc4820000, v76
	v_add_u32_e32 v77, 0xc4820000, v77
	v_add_u32_e32 v78, 0xc4820000, v78
	v_add_u32_e32 v79, 0xc4820000, v79
	v_add_u32_e32 v72, 0xc4820000, v72
	v_add_u32_e32 v73, 0xc4820000, v73
	v_add_u32_e32 v74, 0xc4820000, v74
	v_add_u32_e32 v75, 0xc4820000, v75
	v_add_u32_e32 v68, 0xc4820000, v68
	v_add_u32_e32 v69, 0xc4820000, v69
	v_add_u32_e32 v70, 0xc4820000, v70
	v_add_u32_e32 v71, 0xc4820000, v71
	v_ashrrev_i32_e32 v80, 18, v80
	v_ashrrev_i32_e32 v81, 18, v81
	v_ashrrev_i32_e32 v82, 18, v82
	v_ashrrev_i32_e32 v83, 18, v83
	v_ashrrev_i32_e32 v76, 18, v76
	v_ashrrev_i32_e32 v77, 18, v77
	v_ashrrev_i32_e32 v78, 18, v78
	v_ashrrev_i32_e32 v79, 18, v79
	v_ashrrev_i32_e32 v72, 18, v72
	v_ashrrev_i32_e32 v73, 18, v73
	v_ashrrev_i32_e32 v74, 18, v74
	v_ashrrev_i32_e32 v75, 18, v75
	v_ashrrev_i32_e32 v68, 18, v68
	v_ashrrev_i32_e32 v69, 18, v69
	v_ashrrev_i32_e32 v70, 18, v70
	v_ashrrev_i32_e32 v71, 18, v71
	v_med3_i32 v80, v80, 0, v236
	v_med3_i32 v81, v81, 0, v236
	v_med3_i32 v82, v82, 0, v236
	v_med3_i32 v83, v83, 0, v236
	v_med3_i32 v76, v76, 0, v236
	v_med3_i32 v77, v77, 0, v236
	v_med3_i32 v78, v78, 0, v236
	v_med3_i32 v79, v79, 0, v236
	v_med3_i32 v72, v72, 0, v236
	v_med3_i32 v73, v73, 0, v236
	v_med3_i32 v74, v74, 0, v236
	v_med3_i32 v75, v75, 0, v236
	v_med3_i32 v68, v68, 0, v236
	v_med3_i32 v69, v69, 0, v236
	v_med3_i32 v70, v70, 0, v236
	v_med3_i32 v71, v71, 0, v236
	v_lshl_or_b32 v80, v81, 8, v80
	v_lshl_or_b32 v82, v83, 8, v82
	v_lshl_or_b32 v100, v82, 16, v80
	v_lshl_or_b32 v76, v77, 8, v76
	v_lshl_or_b32 v78, v79, 8, v78
	v_lshl_or_b32 v101, v78, 16, v76
	v_lshl_or_b32 v72, v73, 8, v72
	v_lshl_or_b32 v74, v75, 8, v74
	v_lshl_or_b32 v102, v74, 16, v72
	v_lshl_or_b32 v68, v69, 8, v68
	v_lshl_or_b32 v70, v71, 8, v70
	v_lshl_or_b32 v103, v70, 16, v68
	global_store_dwordx4 v[106:107], v[100:103], off

.LBB0_885:
	s_waitcnt lgkmcnt(1)
	s_waitcnt lgkmcnt(0)
	v_fmamk_f32 v64, v64, 0xbfb8aa3b, v120
	v_fmamk_f32 v65, v65, 0xbfb8aa3b, v121
	v_fmamk_f32 v66, v66, 0xbfb8aa3b, v122
	v_fmamk_f32 v67, v67, 0xbfb8aa3b, v123
	v_fmamk_f32 v60, v60, 0xbfb8aa3b, v116
	v_fmamk_f32 v61, v61, 0xbfb8aa3b, v117
	v_fmamk_f32 v62, v62, 0xbfb8aa3b, v118
	v_fmamk_f32 v63, v63, 0xbfb8aa3b, v119
	v_fmamk_f32 v56, v56, 0xbfb8aa3b, v124
	v_fmamk_f32 v57, v57, 0xbfb8aa3b, v125
	v_fmamk_f32 v58, v58, 0xbfb8aa3b, v126
	v_fmamk_f32 v59, v59, 0xbfb8aa3b, v127
	v_fmamk_f32 v52, v52, 0xbfb8aa3b, v128
	v_fmamk_f32 v53, v53, 0xbfb8aa3b, v129
	v_fmamk_f32 v54, v54, 0xbfb8aa3b, v130
	v_fmamk_f32 v55, v55, 0xbfb8aa3b, v131
	v_mov_b32_e32 v133, v142
	s_add_i32 s19, s87, -11
	s_lshr_b32 s20, s19, 2
	v_mov_b32_e32 v120, s20
	v_mov_b32_e32 v121, v3
	v_mad_i64_i32 v[120:121], s[20:21], v138, 3, v[120:121]
	v_lshlrev_b64 v[120:121], 10, v[120:121]
	s_lshl_b32 s19, s19, 8
	s_and_b32 s34, s19, 0x300
	v_lshl_add_u64 v[120:121], s[46:47], 0, v[120:121]
	v_lshl_add_u64 v[120:121], v[120:121], 0, s[34:35]
	v_lshl_add_u64 v[122:123], v[120:121], 0, v[2:3]
	v_exp_f32_e32 v64, v64
	v_exp_f32_e32 v65, v65
	v_exp_f32_e32 v66, v66
	v_exp_f32_e32 v67, v67
	v_exp_f32_e32 v60, v60
	v_exp_f32_e32 v61, v61
	v_exp_f32_e32 v62, v62
	v_exp_f32_e32 v63, v63
	v_exp_f32_e32 v56, v56
	v_exp_f32_e32 v57, v57
	v_exp_f32_e32 v58, v58
	v_exp_f32_e32 v59, v59
	v_exp_f32_e32 v52, v52
	v_exp_f32_e32 v53, v53
	v_exp_f32_e32 v54, v54
	v_exp_f32_e32 v55, v55
	v_add_f32_e32 v64, 1.0, v64
	v_add_f32_e32 v65, 1.0, v65
	v_add_f32_e32 v66, 1.0, v66
	v_add_f32_e32 v67, 1.0, v67
	v_add_f32_e32 v60, 1.0, v60
	v_add_f32_e32 v61, 1.0, v61
	v_add_f32_e32 v62, 1.0, v62
	v_add_f32_e32 v63, 1.0, v63
	v_add_f32_e32 v56, 1.0, v56
	v_add_f32_e32 v57, 1.0, v57
	v_add_f32_e32 v58, 1.0, v58
	v_add_f32_e32 v59, 1.0, v59
	v_add_f32_e32 v52, 1.0, v52
	v_add_f32_e32 v53, 1.0, v53
	v_add_f32_e32 v54, 1.0, v54
	v_add_f32_e32 v55, 1.0, v55
	v_rcp_f32_e32 v64, v64
	v_rcp_f32_e32 v65, v65
	v_rcp_f32_e32 v66, v66
	v_rcp_f32_e32 v67, v67
	v_rcp_f32_e32 v60, v60
	v_rcp_f32_e32 v61, v61
	v_rcp_f32_e32 v62, v62
	v_rcp_f32_e32 v63, v63
	v_rcp_f32_e32 v56, v56
	v_rcp_f32_e32 v57, v57
	v_rcp_f32_e32 v58, v58
	v_rcp_f32_e32 v59, v59
	v_rcp_f32_e32 v52, v52
	v_rcp_f32_e32 v53, v53
	v_rcp_f32_e32 v54, v54
	v_rcp_f32_e32 v55, v55
	v_add_u32_e32 v64, 0xc4820000, v64
	v_add_u32_e32 v65, 0xc4820000, v65
	v_add_u32_e32 v66, 0xc4820000, v66
	v_add_u32_e32 v67, 0xc4820000, v67
	v_add_u32_e32 v60, 0xc4820000, v60
	v_add_u32_e32 v61, 0xc4820000, v61
	v_add_u32_e32 v62, 0xc4820000, v62
	v_add_u32_e32 v63, 0xc4820000, v63
	v_add_u32_e32 v56, 0xc4820000, v56
	v_add_u32_e32 v57, 0xc4820000, v57
	v_add_u32_e32 v58, 0xc4820000, v58
	v_add_u32_e32 v59, 0xc4820000, v59
	v_add_u32_e32 v52, 0xc4820000, v52
	v_add_u32_e32 v53, 0xc4820000, v53
	v_add_u32_e32 v54, 0xc4820000, v54
	v_add_u32_e32 v55, 0xc4820000, v55
	v_ashrrev_i32_e32 v64, 18, v64
	v_ashrrev_i32_e32 v65, 18, v65
	v_ashrrev_i32_e32 v66, 18, v66
	v_ashrrev_i32_e32 v67, 18, v67
	v_ashrrev_i32_e32 v60, 18, v60
	v_ashrrev_i32_e32 v61, 18, v61
	v_ashrrev_i32_e32 v62, 18, v62
	v_ashrrev_i32_e32 v63, 18, v63
	v_ashrrev_i32_e32 v56, 18, v56
	v_ashrrev_i32_e32 v57, 18, v57
	v_ashrrev_i32_e32 v58, 18, v58
	v_ashrrev_i32_e32 v59, 18, v59
	v_ashrrev_i32_e32 v52, 18, v52
	v_ashrrev_i32_e32 v53, 18, v53
	v_ashrrev_i32_e32 v54, 18, v54
	v_ashrrev_i32_e32 v55, 18, v55
	v_med3_i32 v64, v64, 0, v236
	v_med3_i32 v65, v65, 0, v236
	v_med3_i32 v66, v66, 0, v236
	v_med3_i32 v67, v67, 0, v236
	v_med3_i32 v60, v60, 0, v236
	v_med3_i32 v61, v61, 0, v236
	v_med3_i32 v62, v62, 0, v236
	v_med3_i32 v63, v63, 0, v236
	v_med3_i32 v56, v56, 0, v236
	v_med3_i32 v57, v57, 0, v236
	v_med3_i32 v58, v58, 0, v236
	v_med3_i32 v59, v59, 0, v236
	v_med3_i32 v52, v52, 0, v236
	v_med3_i32 v53, v53, 0, v236
	v_med3_i32 v54, v54, 0, v236
	v_med3_i32 v55, v55, 0, v236
	v_lshl_or_b32 v64, v65, 8, v64
	v_lshl_or_b32 v66, v67, 8, v66
	v_lshl_or_b32 v116, v66, 16, v64
	v_lshl_or_b32 v60, v61, 8, v60
	v_lshl_or_b32 v62, v63, 8, v62
	v_lshl_or_b32 v117, v62, 16, v60
	v_lshl_or_b32 v56, v57, 8, v56
	v_lshl_or_b32 v58, v59, 8, v58
	v_lshl_or_b32 v118, v58, 16, v56
	v_lshl_or_b32 v52, v53, 8, v52
	v_lshl_or_b32 v54, v55, 8, v54
	v_lshl_or_b32 v119, v54, 16, v52
	global_store_dwordx4 v[122:123], v[116:119], off
	s_and_b64 vcc, exec, s[40:41]
	s_mov_b64 s[26:27], -1
	s_cbranch_vccz .LBB0_950

.LBB0_887:
	s_waitcnt lgkmcnt(1)
	s_waitcnt lgkmcnt(0)
	v_fmamk_f32 v48, v48, 0xbfb8aa3b, v104
	v_fmamk_f32 v49, v49, 0xbfb8aa3b, v105
	v_fmamk_f32 v50, v50, 0xbfb8aa3b, v106
	v_fmamk_f32 v51, v51, 0xbfb8aa3b, v107
	v_fmamk_f32 v44, v44, 0xbfb8aa3b, v100
	v_fmamk_f32 v45, v45, 0xbfb8aa3b, v101
	v_fmamk_f32 v46, v46, 0xbfb8aa3b, v102
	v_fmamk_f32 v47, v47, 0xbfb8aa3b, v103
	v_fmamk_f32 v40, v40, 0xbfb8aa3b, v108
	v_fmamk_f32 v41, v41, 0xbfb8aa3b, v109
	v_fmamk_f32 v42, v42, 0xbfb8aa3b, v110
	v_fmamk_f32 v43, v43, 0xbfb8aa3b, v111
	v_fmamk_f32 v36, v36, 0xbfb8aa3b, v112
	v_fmamk_f32 v37, v37, 0xbfb8aa3b, v113
	v_fmamk_f32 v38, v38, 0xbfb8aa3b, v114
	v_fmamk_f32 v39, v39, 0xbfb8aa3b, v115
	v_mov_b32_e32 v54, v133
	s_add_i32 s19, s87, -11
	s_lshr_b32 s20, s19, 2
	v_mov_b32_e32 v104, s20
	v_mov_b32_e32 v105, v3
	v_mad_i64_i32 v[104:105], s[20:21], v136, 3, v[104:105]
	v_lshlrev_b64 v[104:105], 10, v[104:105]
	s_lshl_b32 s19, s19, 8
	s_and_b32 s34, s19, 0x300
	v_lshl_add_u64 v[104:105], s[46:47], 0, v[104:105]
	v_lshl_add_u64 v[104:105], v[104:105], 0, s[34:35]
	v_lshl_add_u64 v[106:107], v[104:105], 0, v[2:3]
	v_exp_f32_e32 v48, v48
	v_exp_f32_e32 v49, v49
	v_exp_f32_e32 v50, v50
	v_exp_f32_e32 v51, v51
	v_exp_f32_e32 v44, v44
	v_exp_f32_e32 v45, v45
	v_exp_f32_e32 v46, v46
	v_exp_f32_e32 v47, v47
	v_exp_f32_e32 v40, v40
	v_exp_f32_e32 v41, v41
	v_exp_f32_e32 v42, v42
	v_exp_f32_e32 v43, v43
	v_exp_f32_e32 v36, v36
	v_exp_f32_e32 v37, v37
	v_exp_f32_e32 v38, v38
	v_exp_f32_e32 v39, v39
	v_add_f32_e32 v48, 1.0, v48
	v_add_f32_e32 v49, 1.0, v49
	v_add_f32_e32 v50, 1.0, v50
	v_add_f32_e32 v51, 1.0, v51
	v_add_f32_e32 v44, 1.0, v44
	v_add_f32_e32 v45, 1.0, v45
	v_add_f32_e32 v46, 1.0, v46
	v_add_f32_e32 v47, 1.0, v47
	v_add_f32_e32 v40, 1.0, v40
	v_add_f32_e32 v41, 1.0, v41
	v_add_f32_e32 v42, 1.0, v42
	v_add_f32_e32 v43, 1.0, v43
	v_add_f32_e32 v36, 1.0, v36
	v_add_f32_e32 v37, 1.0, v37
	v_add_f32_e32 v38, 1.0, v38
	v_add_f32_e32 v39, 1.0, v39
	v_rcp_f32_e32 v48, v48
	v_rcp_f32_e32 v49, v49
	v_rcp_f32_e32 v50, v50
	v_rcp_f32_e32 v51, v51
	v_rcp_f32_e32 v44, v44
	v_rcp_f32_e32 v45, v45
	v_rcp_f32_e32 v46, v46
	v_rcp_f32_e32 v47, v47
	v_rcp_f32_e32 v40, v40
	v_rcp_f32_e32 v41, v41
	v_rcp_f32_e32 v42, v42
	v_rcp_f32_e32 v43, v43
	v_rcp_f32_e32 v36, v36
	v_rcp_f32_e32 v37, v37
	v_rcp_f32_e32 v38, v38
	v_rcp_f32_e32 v39, v39
	v_add_u32_e32 v48, 0xc4820000, v48
	v_add_u32_e32 v49, 0xc4820000, v49
	v_add_u32_e32 v50, 0xc4820000, v50
	v_add_u32_e32 v51, 0xc4820000, v51
	v_add_u32_e32 v44, 0xc4820000, v44
	v_add_u32_e32 v45, 0xc4820000, v45
	v_add_u32_e32 v46, 0xc4820000, v46
	v_add_u32_e32 v47, 0xc4820000, v47
	v_add_u32_e32 v40, 0xc4820000, v40
	v_add_u32_e32 v41, 0xc4820000, v41
	v_add_u32_e32 v42, 0xc4820000, v42
	v_add_u32_e32 v43, 0xc4820000, v43
	v_add_u32_e32 v36, 0xc4820000, v36
	v_add_u32_e32 v37, 0xc4820000, v37
	v_add_u32_e32 v38, 0xc4820000, v38
	v_add_u32_e32 v39, 0xc4820000, v39
	v_ashrrev_i32_e32 v48, 18, v48
	v_ashrrev_i32_e32 v49, 18, v49
	v_ashrrev_i32_e32 v50, 18, v50
	v_ashrrev_i32_e32 v51, 18, v51
	v_ashrrev_i32_e32 v44, 18, v44
	v_ashrrev_i32_e32 v45, 18, v45
	v_ashrrev_i32_e32 v46, 18, v46
	v_ashrrev_i32_e32 v47, 18, v47
	v_ashrrev_i32_e32 v40, 18, v40
	v_ashrrev_i32_e32 v41, 18, v41
	v_ashrrev_i32_e32 v42, 18, v42
	v_ashrrev_i32_e32 v43, 18, v43
	v_ashrrev_i32_e32 v36, 18, v36
	v_ashrrev_i32_e32 v37, 18, v37
	v_ashrrev_i32_e32 v38, 18, v38
	v_ashrrev_i32_e32 v39, 18, v39
	v_med3_i32 v48, v48, 0, v236
	v_med3_i32 v49, v49, 0, v236
	v_med3_i32 v50, v50, 0, v236
	v_med3_i32 v51, v51, 0, v236
	v_med3_i32 v44, v44, 0, v236
	v_med3_i32 v45, v45, 0, v236
	v_med3_i32 v46, v46, 0, v236
	v_med3_i32 v47, v47, 0, v236
	v_med3_i32 v40, v40, 0, v236
	v_med3_i32 v41, v41, 0, v236
	v_med3_i32 v42, v42, 0, v236
	v_med3_i32 v43, v43, 0, v236
	v_med3_i32 v36, v36, 0, v236
	v_med3_i32 v37, v37, 0, v236
	v_med3_i32 v38, v38, 0, v236
	v_med3_i32 v39, v39, 0, v236
	v_lshl_or_b32 v48, v49, 8, v48
	v_lshl_or_b32 v50, v51, 8, v50
	v_lshl_or_b32 v100, v50, 16, v48
	v_lshl_or_b32 v44, v45, 8, v44
	v_lshl_or_b32 v46, v47, 8, v46
	v_lshl_or_b32 v101, v46, 16, v44
	v_lshl_or_b32 v40, v41, 8, v40
	v_lshl_or_b32 v42, v43, 8, v42
	v_lshl_or_b32 v102, v42, 16, v40
	v_lshl_or_b32 v36, v37, 8, v36
	v_lshl_or_b32 v38, v39, 8, v38
	v_lshl_or_b32 v103, v38, 16, v36
	global_store_dwordx4 v[106:107], v[100:103], off
	s_and_b64 vcc, exec, s[40:41]
	s_mov_b64 s[26:27], -1
	s_cbranch_vccz .LBB0_1000

.LBB0_889:
	s_waitcnt lgkmcnt(1)
	s_waitcnt lgkmcnt(0)
	v_fmamk_f32 v32, v32, 0xbfb8aa3b, v88
	v_fmamk_f32 v33, v33, 0xbfb8aa3b, v89
	v_fmamk_f32 v34, v34, 0xbfb8aa3b, v90
	v_fmamk_f32 v35, v35, 0xbfb8aa3b, v91
	v_fmamk_f32 v28, v28, 0xbfb8aa3b, v84
	v_fmamk_f32 v29, v29, 0xbfb8aa3b, v85
	v_fmamk_f32 v30, v30, 0xbfb8aa3b, v86
	v_fmamk_f32 v31, v31, 0xbfb8aa3b, v87
	v_fmamk_f32 v24, v24, 0xbfb8aa3b, v92
	v_fmamk_f32 v25, v25, 0xbfb8aa3b, v93
	v_fmamk_f32 v26, v26, 0xbfb8aa3b, v94
	v_fmamk_f32 v27, v27, 0xbfb8aa3b, v95
	v_fmamk_f32 v20, v20, 0xbfb8aa3b, v96
	v_fmamk_f32 v21, v21, 0xbfb8aa3b, v97
	v_fmamk_f32 v22, v22, 0xbfb8aa3b, v98
	v_fmamk_f32 v23, v23, 0xbfb8aa3b, v99
	v_mov_b32_e32 v38, v54
	s_add_i32 s19, s87, -11
	s_lshr_b32 s20, s19, 2
	v_mov_b32_e32 v88, s20
	v_mov_b32_e32 v89, v3
	v_mad_i64_i32 v[88:89], s[20:21], v134, 3, v[88:89]
	v_lshlrev_b64 v[88:89], 10, v[88:89]
	s_lshl_b32 s19, s19, 8
	s_and_b32 s34, s19, 0x300
	v_lshl_add_u64 v[88:89], s[46:47], 0, v[88:89]
	v_lshl_add_u64 v[88:89], v[88:89], 0, s[34:35]
	v_lshl_add_u64 v[90:91], v[88:89], 0, v[2:3]
	v_exp_f32_e32 v32, v32
	v_exp_f32_e32 v33, v33
	v_exp_f32_e32 v34, v34
	v_exp_f32_e32 v35, v35
	v_exp_f32_e32 v28, v28
	v_exp_f32_e32 v29, v29
	v_exp_f32_e32 v30, v30
	v_exp_f32_e32 v31, v31
	v_exp_f32_e32 v24, v24
	v_exp_f32_e32 v25, v25
	v_exp_f32_e32 v26, v26
	v_exp_f32_e32 v27, v27
	v_exp_f32_e32 v20, v20
	v_exp_f32_e32 v21, v21
	v_exp_f32_e32 v22, v22
	v_exp_f32_e32 v23, v23
	v_add_f32_e32 v32, 1.0, v32
	v_add_f32_e32 v33, 1.0, v33
	v_add_f32_e32 v34, 1.0, v34
	v_add_f32_e32 v35, 1.0, v35
	v_add_f32_e32 v28, 1.0, v28
	v_add_f32_e32 v29, 1.0, v29
	v_add_f32_e32 v30, 1.0, v30
	v_add_f32_e32 v31, 1.0, v31
	v_add_f32_e32 v24, 1.0, v24
	v_add_f32_e32 v25, 1.0, v25
	v_add_f32_e32 v26, 1.0, v26
	v_add_f32_e32 v27, 1.0, v27
	v_add_f32_e32 v20, 1.0, v20
	v_add_f32_e32 v21, 1.0, v21
	v_add_f32_e32 v22, 1.0, v22
	v_add_f32_e32 v23, 1.0, v23
	v_rcp_f32_e32 v32, v32
	v_rcp_f32_e32 v33, v33
	v_rcp_f32_e32 v34, v34
	v_rcp_f32_e32 v35, v35
	v_rcp_f32_e32 v28, v28
	v_rcp_f32_e32 v29, v29
	v_rcp_f32_e32 v30, v30
	v_rcp_f32_e32 v31, v31
	v_rcp_f32_e32 v24, v24
	v_rcp_f32_e32 v25, v25
	v_rcp_f32_e32 v26, v26
	v_rcp_f32_e32 v27, v27
	v_rcp_f32_e32 v20, v20
	v_rcp_f32_e32 v21, v21
	v_rcp_f32_e32 v22, v22
	v_rcp_f32_e32 v23, v23
	v_add_u32_e32 v32, 0xc4820000, v32
	v_add_u32_e32 v33, 0xc4820000, v33
	v_add_u32_e32 v34, 0xc4820000, v34
	v_add_u32_e32 v35, 0xc4820000, v35
	v_add_u32_e32 v28, 0xc4820000, v28
	v_add_u32_e32 v29, 0xc4820000, v29
	v_add_u32_e32 v30, 0xc4820000, v30
	v_add_u32_e32 v31, 0xc4820000, v31
	v_add_u32_e32 v24, 0xc4820000, v24
	v_add_u32_e32 v25, 0xc4820000, v25
	v_add_u32_e32 v26, 0xc4820000, v26
	v_add_u32_e32 v27, 0xc4820000, v27
	v_add_u32_e32 v20, 0xc4820000, v20
	v_add_u32_e32 v21, 0xc4820000, v21
	v_add_u32_e32 v22, 0xc4820000, v22
	v_add_u32_e32 v23, 0xc4820000, v23
	v_ashrrev_i32_e32 v32, 18, v32
	v_ashrrev_i32_e32 v33, 18, v33
	v_ashrrev_i32_e32 v34, 18, v34
	v_ashrrev_i32_e32 v35, 18, v35
	v_ashrrev_i32_e32 v28, 18, v28
	v_ashrrev_i32_e32 v29, 18, v29
	v_ashrrev_i32_e32 v30, 18, v30
	v_ashrrev_i32_e32 v31, 18, v31
	v_ashrrev_i32_e32 v24, 18, v24
	v_ashrrev_i32_e32 v25, 18, v25
	v_ashrrev_i32_e32 v26, 18, v26
	v_ashrrev_i32_e32 v27, 18, v27
	v_ashrrev_i32_e32 v20, 18, v20
	v_ashrrev_i32_e32 v21, 18, v21
	v_ashrrev_i32_e32 v22, 18, v22
	v_ashrrev_i32_e32 v23, 18, v23
	v_med3_i32 v32, v32, 0, v236
	v_med3_i32 v33, v33, 0, v236
	v_med3_i32 v34, v34, 0, v236
	v_med3_i32 v35, v35, 0, v236
	v_med3_i32 v28, v28, 0, v236
	v_med3_i32 v29, v29, 0, v236
	v_med3_i32 v30, v30, 0, v236
	v_med3_i32 v31, v31, 0, v236
	v_med3_i32 v24, v24, 0, v236
	v_med3_i32 v25, v25, 0, v236
	v_med3_i32 v26, v26, 0, v236
	v_med3_i32 v27, v27, 0, v236
	v_med3_i32 v20, v20, 0, v236
	v_med3_i32 v21, v21, 0, v236
	v_med3_i32 v22, v22, 0, v236
	v_med3_i32 v23, v23, 0, v236
	v_lshl_or_b32 v32, v33, 8, v32
	v_lshl_or_b32 v34, v35, 8, v34
	v_lshl_or_b32 v84, v34, 16, v32
	v_lshl_or_b32 v28, v29, 8, v28
	v_lshl_or_b32 v30, v31, 8, v30
	v_lshl_or_b32 v85, v30, 16, v28
	v_lshl_or_b32 v24, v25, 8, v24
	v_lshl_or_b32 v26, v27, 8, v26
	v_lshl_or_b32 v86, v26, 16, v24
	v_lshl_or_b32 v20, v21, 8, v20
	v_lshl_or_b32 v22, v23, 8, v22
	v_lshl_or_b32 v87, v22, 16, v20
	global_store_dwordx4 v[90:91], v[84:87], off
	s_and_b64 vcc, exec, s[40:41]
	s_mov_b64 s[26:27], -1
	s_cbranch_vccz .LBB0_1050

.LBB0_891:
	s_waitcnt lgkmcnt(1)
	s_waitcnt lgkmcnt(0)
	v_fmamk_f32 v16, v16, 0xbfb8aa3b, v72
	v_fmamk_f32 v17, v17, 0xbfb8aa3b, v73
	v_fmamk_f32 v18, v18, 0xbfb8aa3b, v74
	v_fmamk_f32 v19, v19, 0xbfb8aa3b, v75
	v_fmamk_f32 v12, v12, 0xbfb8aa3b, v68
	v_fmamk_f32 v13, v13, 0xbfb8aa3b, v69
	v_fmamk_f32 v14, v14, 0xbfb8aa3b, v70
	v_fmamk_f32 v15, v15, 0xbfb8aa3b, v71
	v_fmamk_f32 v8, v8, 0xbfb8aa3b, v76
	v_fmamk_f32 v9, v9, 0xbfb8aa3b, v77
	v_fmamk_f32 v10, v10, 0xbfb8aa3b, v78
	v_fmamk_f32 v11, v11, 0xbfb8aa3b, v79
	v_fmamk_f32 v4, v4, 0xbfb8aa3b, v80
	v_fmamk_f32 v5, v5, 0xbfb8aa3b, v81
	v_fmamk_f32 v6, v6, 0xbfb8aa3b, v82
	v_fmamk_f32 v7, v7, 0xbfb8aa3b, v83
	v_mov_b32_e32 v28, v38
	s_add_i32 s87, s87, -11
	s_lshr_b32 s19, s87, 2
	v_mov_b32_e32 v72, s19
	v_mov_b32_e32 v73, v3
	v_mad_i64_i32 v[72:73], s[20:21], v132, 3, v[72:73]
	v_lshlrev_b64 v[72:73], 10, v[72:73]
	s_lshl_b32 s19, s87, 8
	s_and_b32 s34, s19, 0x300
	v_lshl_add_u64 v[72:73], s[46:47], 0, v[72:73]
	v_lshl_add_u64 v[72:73], v[72:73], 0, s[34:35]
	v_lshl_add_u64 v[74:75], v[72:73], 0, v[2:3]
	v_exp_f32_e32 v16, v16
	v_exp_f32_e32 v17, v17
	v_exp_f32_e32 v18, v18
	v_exp_f32_e32 v19, v19
	v_exp_f32_e32 v12, v12
	v_exp_f32_e32 v13, v13
	v_exp_f32_e32 v14, v14
	v_exp_f32_e32 v15, v15
	v_exp_f32_e32 v8, v8
	v_exp_f32_e32 v9, v9
	v_exp_f32_e32 v10, v10
	v_exp_f32_e32 v11, v11
	v_exp_f32_e32 v4, v4
	v_exp_f32_e32 v5, v5
	v_exp_f32_e32 v6, v6
	v_exp_f32_e32 v7, v7
	v_add_f32_e32 v16, 1.0, v16
	v_add_f32_e32 v17, 1.0, v17
	v_add_f32_e32 v18, 1.0, v18
	v_add_f32_e32 v19, 1.0, v19
	v_add_f32_e32 v12, 1.0, v12
	v_add_f32_e32 v13, 1.0, v13
	v_add_f32_e32 v14, 1.0, v14
	v_add_f32_e32 v15, 1.0, v15
	v_add_f32_e32 v8, 1.0, v8
	v_add_f32_e32 v9, 1.0, v9
	v_add_f32_e32 v10, 1.0, v10
	v_add_f32_e32 v11, 1.0, v11
	v_add_f32_e32 v4, 1.0, v4
	v_add_f32_e32 v5, 1.0, v5
	v_add_f32_e32 v6, 1.0, v6
	v_add_f32_e32 v7, 1.0, v7
	v_rcp_f32_e32 v16, v16
	v_rcp_f32_e32 v17, v17
	v_rcp_f32_e32 v18, v18
	v_rcp_f32_e32 v19, v19
	v_rcp_f32_e32 v12, v12
	v_rcp_f32_e32 v13, v13
	v_rcp_f32_e32 v14, v14
	v_rcp_f32_e32 v15, v15
	v_rcp_f32_e32 v8, v8
	v_rcp_f32_e32 v9, v9
	v_rcp_f32_e32 v10, v10
	v_rcp_f32_e32 v11, v11
	v_rcp_f32_e32 v4, v4
	v_rcp_f32_e32 v5, v5
	v_rcp_f32_e32 v6, v6
	v_rcp_f32_e32 v7, v7
	v_add_u32_e32 v16, 0xc4820000, v16
	v_add_u32_e32 v17, 0xc4820000, v17
	v_add_u32_e32 v18, 0xc4820000, v18
	v_add_u32_e32 v19, 0xc4820000, v19
	v_add_u32_e32 v12, 0xc4820000, v12
	v_add_u32_e32 v13, 0xc4820000, v13
	v_add_u32_e32 v14, 0xc4820000, v14
	v_add_u32_e32 v15, 0xc4820000, v15
	v_add_u32_e32 v8, 0xc4820000, v8
	v_add_u32_e32 v9, 0xc4820000, v9
	v_add_u32_e32 v10, 0xc4820000, v10
	v_add_u32_e32 v11, 0xc4820000, v11
	v_add_u32_e32 v4, 0xc4820000, v4
	v_add_u32_e32 v5, 0xc4820000, v5
	v_add_u32_e32 v6, 0xc4820000, v6
	v_add_u32_e32 v7, 0xc4820000, v7
	v_ashrrev_i32_e32 v16, 18, v16
	v_ashrrev_i32_e32 v17, 18, v17
	v_ashrrev_i32_e32 v18, 18, v18
	v_ashrrev_i32_e32 v19, 18, v19
	v_ashrrev_i32_e32 v12, 18, v12
	v_ashrrev_i32_e32 v13, 18, v13
	v_ashrrev_i32_e32 v14, 18, v14
	v_ashrrev_i32_e32 v15, 18, v15
	v_ashrrev_i32_e32 v8, 18, v8
	v_ashrrev_i32_e32 v9, 18, v9
	v_ashrrev_i32_e32 v10, 18, v10
	v_ashrrev_i32_e32 v11, 18, v11
	v_ashrrev_i32_e32 v4, 18, v4
	v_ashrrev_i32_e32 v5, 18, v5
	v_ashrrev_i32_e32 v6, 18, v6
	v_ashrrev_i32_e32 v7, 18, v7
	v_med3_i32 v16, v16, 0, v236
	v_med3_i32 v17, v17, 0, v236
	v_med3_i32 v18, v18, 0, v236
	v_med3_i32 v19, v19, 0, v236
	v_med3_i32 v12, v12, 0, v236
	v_med3_i32 v13, v13, 0, v236
	v_med3_i32 v14, v14, 0, v236
	v_med3_i32 v15, v15, 0, v236
	v_med3_i32 v8, v8, 0, v236
	v_med3_i32 v9, v9, 0, v236
	v_med3_i32 v10, v10, 0, v236
	v_med3_i32 v11, v11, 0, v236
	v_med3_i32 v4, v4, 0, v236
	v_med3_i32 v5, v5, 0, v236
	v_med3_i32 v6, v6, 0, v236
	v_med3_i32 v7, v7, 0, v236
	v_lshl_or_b32 v16, v17, 8, v16
	v_lshl_or_b32 v18, v19, 8, v18
	v_lshl_or_b32 v68, v18, 16, v16
	v_lshl_or_b32 v12, v13, 8, v12
	v_lshl_or_b32 v14, v15, 8, v14
	v_lshl_or_b32 v69, v14, 16, v12
	v_lshl_or_b32 v8, v9, 8, v8
	v_lshl_or_b32 v10, v11, 8, v10
	v_lshl_or_b32 v70, v10, 16, v8
	v_lshl_or_b32 v4, v5, 8, v4
	v_lshl_or_b32 v6, v7, 8, v6
	v_lshl_or_b32 v71, v6, 16, v4
	global_store_dwordx4 v[74:75], v[68:71], off
